# P7/P8 unit scheduling: expert lookup by one per-lane LDS read + compare + popcount instead of a chain of up to 16 dependent LDS round trips before every unit
# speedup vs baseline: 1.0088x; 1.0084x over previous
.LBB0_1184:
	s_lshl_b32 s24, s34, 3
	s_and_b64 vcc, exec, s[0:1]
	s_cbranch_vccz .LBB0_1189
	s_cmp_ge_i32 s4, s24
	s_cbranch_scc1 .LBB0_1187
	s_ashr_i32 s0, s4, 31
	s_lshr_b32 s0, s0, 29
	s_add_i32 s0, s4, s0
	s_ashr_i32 s1, s0, 3
	s_lshl_b32 s4, s4, 8
	v_mbcnt_lo_u32_b32 v2, -1, 0
	v_mbcnt_hi_u32_b32 v2, -1, v2
	v_min_u32_e32 v2, 31, v2
	v_lshlrev_b32_e32 v2, 2, v2
	v_add_u32_e32 v2, 0x20490, v2
	ds_read_b32 v2, v2
	s_waitcnt lgkmcnt(0)
	v_cmp_ge_i32_e32 vcc, s1, v2
	s_and_b32 s0, vcc_lo, 0xfffffffe
	s_bcnt1_i32_b32 s0, s0
	s_lshl_b32 s5, s0, 2
	s_add_i32 s5, s5, 0
	s_add_i32 s8, s5, 0x20490
	v_mov_b32_e32 v2, s8
	ds_read_b32 v4, v2
	s_add_i32 s5, s5, 0x20400
	v_mov_b32_e32 v2, s5
	ds_read2_b32 v[2:3], v2 offset1:1
	s_waitcnt lgkmcnt(1)
	v_readfirstlane_b32 s5, v4
	s_sub_i32 s5, s1, s5
	s_lshl_b32 s5, s5, 8
	s_waitcnt lgkmcnt(0)
	v_readfirstlane_b32 s8, v2
	s_sub_i32 s1, s0, s1
	v_readfirstlane_b32 s9, v3
	s_add_i32 s69, s8, s5
	s_lshl_b32 s1, s1, 11
	s_sub_i32 s8, s9, s69
	s_add_i32 s33, s1, s4
	s_lshl_b32 s1, s0, 14
	s_min_i32 s68, s8, 0x100
	s_add_i32 s8, s5, s1
	s_ashr_i32 s1, s0, 31
	s_lshl_b64 s[0:1], s[0:1], 12
	s_mov_b64 s[4:5], -1
	s_branch .LBB0_1190

.LBB0_1203:
	s_mov_b64 s[74:75], 0
	s_and_b64 vcc, exec, s[0:1]
	s_cbranch_vccz .LBB0_1206
	s_cmp_ge_i32 s22, s24
	s_cbranch_scc1 .LBB0_1206
	s_ashr_i32 s0, s22, 31
	s_lshr_b32 s0, s0, 29
	s_add_i32 s0, s22, s0
	s_ashr_i32 s0, s0, 3
	s_mov_b64 s[74:75], -1
	v_mbcnt_lo_u32_b32 v2, -1, 0
	v_mbcnt_hi_u32_b32 v2, -1, v2
	v_min_u32_e32 v2, 31, v2
	v_lshlrev_b32_e32 v2, 2, v2
	v_add_u32_e32 v2, 0x20490, v2
	ds_read_b32 v2, v2
	s_waitcnt lgkmcnt(0)
	v_cmp_ge_i32_e32 vcc, s0, v2
	s_and_b32 s64, vcc_lo, 0xfffffffe
	s_bcnt1_i32_b32 s64, s64
	s_lshl_b32 s1, s64, 2
	s_add_i32 s1, s1, 0
	s_add_i32 s6, s1, 0x20490
	v_mov_b32_e32 v2, s6
	ds_read_b32 v2, v2
	s_add_i32 s1, s1, 0x20400
	s_waitcnt lgkmcnt(0)
	v_readfirstlane_b32 s6, v2
	v_mov_b32_e32 v2, s1
	ds_read2_b32 v[134:135], v2 offset1:1
	s_sub_i32 s6, s0, s6
	s_lshl_b32 s6, s6, 8
	s_sub_i32 s0, s64, s0
	s_lshl_b32 s0, s0, 11
	s_waitcnt lgkmcnt(0)
	v_readfirstlane_b32 s1, v134
	v_readfirstlane_b32 s7, v135
	s_add_i32 s13, s1, s6
	s_sub_i32 s1, s7, s13
	s_min_i32 s12, s1, 0x100
	s_lshl_b32 s1, s22, 8
	s_add_i32 s82, s0, s1
	s_lshl_b32 s0, s64, 14
	s_add_i32 s70, s6, s0

.LBB0_1288:
	s_and_b64 vcc, exec, s[2:3]
	s_cbranch_vccz .LBB0_1293
	v_readlane_b32 s3, v255, 7
	s_cmp_ge_i32 s3, s34
	s_cbranch_scc1 .LBB0_1291
	s_ashr_i32 s1, s3, 31
	s_lshr_b32 s1, s1, 30
	s_add_i32 s1, s3, s1
	s_ashr_i32 s1, s1, 2
	s_mov_b32 s8, s3
	v_mbcnt_lo_u32_b32 v2, -1, 0
	v_mbcnt_hi_u32_b32 v2, -1, v2
	v_min_u32_e32 v2, 31, v2
	v_lshlrev_b32_e32 v2, 2, v2
	v_add_u32_e32 v2, 0x20490, v2
	ds_read_b32 v2, v2
	s_waitcnt lgkmcnt(0)
	v_cmp_ge_i32_e32 vcc, s1, v2
	s_and_b32 s2, vcc_lo, 0xfffffffe
	s_bcnt1_i32_b32 s2, s2
	s_lshl_b32 s3, s2, 2
	s_add_i32 s3, s3, 0
	s_add_i32 s4, s3, 0x20490
	v_mov_b32_e32 v2, s4
	ds_read_b32 v4, v2
	s_add_i32 s3, s3, 0x20400
	v_mov_b32_e32 v2, s3
	ds_read2_b32 v[2:3], v2 offset1:1
	s_waitcnt lgkmcnt(0)
	v_readfirstlane_b32 s3, v4
	s_sub_i32 s3, s1, s3
	s_lshl_b32 s3, s3, 8
	v_readfirstlane_b32 s4, v2
	v_readfirstlane_b32 s5, v3
	s_add_i32 s62, s4, s3
	s_sub_i32 s3, s5, s62
	s_sub_i32 s1, s2, s1
	s_min_i32 s35, s3, 0x100
	s_lshl_b32 s1, s1, 10
	s_lshl_b32 s3, s8, 8
	s_add_i32 s81, s1, s3
	s_ashr_i32 s3, s2, 31
	s_lshl_b64 s[2:3], s[2:3], 12
	s_mov_b64 s[4:5], -1
	s_branch .LBB0_1294

.LBB0_1307:
	s_mov_b64 s[0:1], -1
	s_and_b64 vcc, exec, s[2:3]
	s_cbranch_vccz .LBB0_1310
	s_cmp_ge_i32 s4, s34
	s_cbranch_scc1 .LBB0_1310
	s_ashr_i32 s0, s4, 31
	s_lshr_b32 s0, s0, 30
	s_add_i32 s0, s4, s0
	s_ashr_i32 s0, s0, 2
	v_mbcnt_lo_u32_b32 v0, -1, 0
	v_mbcnt_hi_u32_b32 v0, -1, v0
	v_min_u32_e32 v0, 31, v0
	v_lshlrev_b32_e32 v0, 2, v0
	v_add_u32_e32 v0, 0x20490, v0
	ds_read_b32 v0, v0
	s_waitcnt lgkmcnt(0)
	v_cmp_ge_i32_e32 vcc, s0, v0
	s_and_b32 s46, vcc_lo, 0xfffffffe
	s_bcnt1_i32_b32 s46, s46
	s_lshl_b32 s1, s46, 2
	s_add_i32 s1, s1, 0
	s_add_i32 s2, s1, 0x20490
	v_mov_b32_e32 v0, s2
	ds_read_b32 v2, v0
	s_add_i32 s1, s1, 0x20400
	v_mov_b32_e32 v0, s1
	ds_read2_b32 v[0:1], v0 offset1:1
	s_waitcnt lgkmcnt(0)
	v_readfirstlane_b32 s1, v2
	s_sub_i32 s1, s0, s1
	s_lshl_b32 s1, s1, 8
	v_readfirstlane_b32 s2, v0
	v_readfirstlane_b32 s3, v1
	s_add_i32 s80, s2, s1
	s_sub_i32 s1, s3, s80
	s_sub_i32 s0, s46, s0
	s_min_i32 s79, s1, 0x100
	s_lshl_b32 s0, s0, 10
	s_lshl_b32 s1, s4, 8
	s_add_i32 s63, s0, s1
	s_mov_b64 s[0:1], 0
